# DSA select scan: two 128-key groups per pass with interleaved dependent chains (ILP), absolute list positions, ballots from SGPR masks; fast path when both groups are inside the row (on top of v048)
# speedup vs baseline: 1.0035x; 1.0017x over previous
.LBB0_1132:
	s_add_i32 s8, s33, 0x100
	s_cmp_gt_i32 s8, s10
	s_cbranch_scc1 .Lsel0_single_0
	s_movk_i32 s96, 0x2c0
	v_and_b32_e32 v7, 0xffff, v63
	v_and_b32_e32 v13, 0xffff, v62
	v_add_u32_e32 v6, 0x80, v2
	v_add_u32_e32 v12, 0x100, v2
	v_lshrrev_b32_e32 v5, 16, v63
	v_lshrrev_b32_e32 v11, 16, v62
	v_cmp_gt_u32_e64 s[44:45], s11, v6
	v_cmp_le_u32_e32 vcc, s93, v7
	v_cmp_le_u32_e64 s[46:47], s93, v5
	v_cmp_gt_u32_e64 s[98:99], s11, v12
	s_and_b64 s[18:19], s[44:45], vcc
	s_and_b64 s[8:9], s[44:45], s[46:47]
	v_cmp_le_u32_e32 vcc, s93, v13
	v_cmp_le_u32_e64 s[44:45], s93, v11
	v_mbcnt_lo_u32_b32 v3, s18, 0
	v_mbcnt_hi_u32_b32 v3, s19, v3
	s_and_b64 s[46:47], s[98:99], vcc
	s_and_b64 s[58:59], s[98:99], s[44:45]
	v_mbcnt_lo_u32_b32 v3, s8, v3
	v_mbcnt_hi_u32_b32 v3, s9, v3
	s_bcnt1_i32_b64 s98, s[18:19]
	s_bcnt1_i32_b64 s99, s[8:9]
	v_mbcnt_lo_u32_b32 v9, s46, 0
	v_mbcnt_hi_u32_b32 v9, s47, v9
	s_add_i32 s98, s98, s99
	v_mbcnt_lo_u32_b32 v9, s58, v9
	v_mbcnt_hi_u32_b32 v9, s59, v9
	v_add_u32_e32 v3, s49, v3
	s_add_i32 s98, s49, s98
	v_cndmask_b32_e64 v0, 0, 1, s[18:19]
	v_add_u32_e32 v9, s98, v9
	v_cndmask_b32_e64 v8, 0, 1, s[46:47]
	v_add_u32_e32 v0, v3, v0
	v_add_u32_e32 v8, v9, v8
	v_cmp_gt_u32_e64 s[44:45], s96, v3
	v_cmp_gt_u32_e64 s[100:101], s96, v0
	v_cmp_gt_u32_e32 vcc, s96, v9
	s_and_b64 s[18:19], s[18:19], s[44:45]
	s_and_saveexec_b64 s[44:45], s[18:19]
	v_lshl_add_u32 v14, v3, 3, s88
	ds_write_b64 v14, v[6:7]
	s_or_b64 exec, exec, s[44:45]
	s_and_b64 s[8:9], s[8:9], s[100:101]
	v_cmp_gt_u32_e64 s[100:101], s96, v8
	s_and_saveexec_b64 s[44:45], s[8:9]
	v_lshl_add_u32 v14, v0, 3, s88
	v_add_u32_e32 v4, 0x81, v2
	ds_write_b64 v14, v[4:5]
	s_or_b64 exec, exec, s[44:45]
	s_bcnt1_i32_b64 s8, s[46:47]
	s_bcnt1_i32_b64 s9, s[58:59]
	s_and_b64 s[46:47], s[46:47], vcc
	s_and_saveexec_b64 s[44:45], s[46:47]
	v_lshl_add_u32 v14, v9, 3, s88
	ds_write_b64 v14, v[12:13]
	s_or_b64 exec, exec, s[44:45]
	s_and_b64 s[58:59], s[58:59], s[100:101]
	s_and_saveexec_b64 s[44:45], s[58:59]
	v_lshl_add_u32 v14, v8, 3, s88
	v_add_u32_e32 v10, 0x101, v2
	ds_write_b64 v14, v[10:11]
	s_or_b64 exec, exec, s[44:45]
	s_add_i32 s8, s8, s9
	s_add_i32 s49, s98, s8
	s_branch .Lsel0_post_0

.Lsel0_post_0:
	s_add_i32 s8, s33, 0x180
	s_cmp_gt_i32 s8, s10
	s_cbranch_scc1 .LBB0_1115
.LBB0_1142:
	s_add_i32 s8, s33, 0x200
	s_cmp_gt_i32 s8, s10
	s_cbranch_scc1 .Lsel0_single_2
	s_movk_i32 s96, 0x2c0
	v_and_b32_e32 v7, 0xffff, v61
	v_and_b32_e32 v13, 0xffff, v58
	v_add_u32_e32 v6, 0x180, v2
	v_add_u32_e32 v12, 0x200, v2
	v_lshrrev_b32_e32 v5, 16, v61
	v_lshrrev_b32_e32 v11, 16, v58
	v_cmp_gt_u32_e64 s[44:45], s11, v6
	v_cmp_le_u32_e32 vcc, s93, v7
	v_cmp_le_u32_e64 s[46:47], s93, v5
	v_cmp_gt_u32_e64 s[98:99], s11, v12
	s_and_b64 s[18:19], s[44:45], vcc
	s_and_b64 s[8:9], s[44:45], s[46:47]
	v_cmp_le_u32_e32 vcc, s93, v13
	v_cmp_le_u32_e64 s[44:45], s93, v11
	v_mbcnt_lo_u32_b32 v3, s18, 0
	v_mbcnt_hi_u32_b32 v3, s19, v3
	s_and_b64 s[46:47], s[98:99], vcc
	s_and_b64 s[58:59], s[98:99], s[44:45]
	v_mbcnt_lo_u32_b32 v3, s8, v3
	v_mbcnt_hi_u32_b32 v3, s9, v3
	s_bcnt1_i32_b64 s98, s[18:19]
	s_bcnt1_i32_b64 s99, s[8:9]
	v_mbcnt_lo_u32_b32 v9, s46, 0
	v_mbcnt_hi_u32_b32 v9, s47, v9
	s_add_i32 s98, s98, s99
	v_mbcnt_lo_u32_b32 v9, s58, v9
	v_mbcnt_hi_u32_b32 v9, s59, v9
	v_add_u32_e32 v3, s49, v3
	s_add_i32 s98, s49, s98
	v_cndmask_b32_e64 v0, 0, 1, s[18:19]
	v_add_u32_e32 v9, s98, v9
	v_cndmask_b32_e64 v8, 0, 1, s[46:47]
	v_add_u32_e32 v0, v3, v0
	v_add_u32_e32 v8, v9, v8
	v_cmp_gt_u32_e64 s[44:45], s96, v3
	v_cmp_gt_u32_e64 s[100:101], s96, v0
	v_cmp_gt_u32_e32 vcc, s96, v9
	s_and_b64 s[18:19], s[18:19], s[44:45]
	s_and_saveexec_b64 s[44:45], s[18:19]
	v_lshl_add_u32 v14, v3, 3, s88
	ds_write_b64 v14, v[6:7]
	s_or_b64 exec, exec, s[44:45]
	s_and_b64 s[8:9], s[8:9], s[100:101]
	v_cmp_gt_u32_e64 s[100:101], s96, v8
	s_and_saveexec_b64 s[44:45], s[8:9]
	v_lshl_add_u32 v14, v0, 3, s88
	v_add_u32_e32 v4, 0x181, v2
	ds_write_b64 v14, v[4:5]
	s_or_b64 exec, exec, s[44:45]
	s_bcnt1_i32_b64 s8, s[46:47]
	s_bcnt1_i32_b64 s9, s[58:59]
	s_and_b64 s[46:47], s[46:47], vcc
	s_and_saveexec_b64 s[44:45], s[46:47]
	v_lshl_add_u32 v14, v9, 3, s88
	ds_write_b64 v14, v[12:13]
	s_or_b64 exec, exec, s[44:45]
	s_and_b64 s[58:59], s[58:59], s[100:101]
	s_and_saveexec_b64 s[44:45], s[58:59]
	v_lshl_add_u32 v14, v8, 3, s88
	v_add_u32_e32 v10, 0x201, v2
	ds_write_b64 v14, v[10:11]
	s_or_b64 exec, exec, s[44:45]
	s_add_i32 s8, s8, s9
	s_add_i32 s49, s98, s8
	s_branch .Lsel0_post_2

.Lsel0_post_2:
	s_add_i32 s8, s33, 0x280
	s_cmp_gt_i32 s8, s10
	s_cbranch_scc1 .LBB0_1117
.LBB0_1152:
	s_add_i32 s8, s33, 0x300
	s_cmp_gt_i32 s8, s10
	s_cbranch_scc1 .Lsel0_single_4
	s_movk_i32 s96, 0x2c0
	v_and_b32_e32 v7, 0xffff, v59
	v_and_b32_e32 v13, 0xffff, v56
	v_add_u32_e32 v6, 0x280, v2
	v_add_u32_e32 v12, 0x300, v2
	v_lshrrev_b32_e32 v5, 16, v59
	v_lshrrev_b32_e32 v11, 16, v56
	v_cmp_gt_u32_e64 s[44:45], s11, v6
	v_cmp_le_u32_e32 vcc, s93, v7
	v_cmp_le_u32_e64 s[46:47], s93, v5
	v_cmp_gt_u32_e64 s[98:99], s11, v12
	s_and_b64 s[18:19], s[44:45], vcc
	s_and_b64 s[8:9], s[44:45], s[46:47]
	v_cmp_le_u32_e32 vcc, s93, v13
	v_cmp_le_u32_e64 s[44:45], s93, v11
	v_mbcnt_lo_u32_b32 v3, s18, 0
	v_mbcnt_hi_u32_b32 v3, s19, v3
	s_and_b64 s[46:47], s[98:99], vcc
	s_and_b64 s[58:59], s[98:99], s[44:45]
	v_mbcnt_lo_u32_b32 v3, s8, v3
	v_mbcnt_hi_u32_b32 v3, s9, v3
	s_bcnt1_i32_b64 s98, s[18:19]
	s_bcnt1_i32_b64 s99, s[8:9]
	v_mbcnt_lo_u32_b32 v9, s46, 0
	v_mbcnt_hi_u32_b32 v9, s47, v9
	s_add_i32 s98, s98, s99
	v_mbcnt_lo_u32_b32 v9, s58, v9
	v_mbcnt_hi_u32_b32 v9, s59, v9
	v_add_u32_e32 v3, s49, v3
	s_add_i32 s98, s49, s98
	v_cndmask_b32_e64 v0, 0, 1, s[18:19]
	v_add_u32_e32 v9, s98, v9
	v_cndmask_b32_e64 v8, 0, 1, s[46:47]
	v_add_u32_e32 v0, v3, v0
	v_add_u32_e32 v8, v9, v8
	v_cmp_gt_u32_e64 s[44:45], s96, v3
	v_cmp_gt_u32_e64 s[100:101], s96, v0
	v_cmp_gt_u32_e32 vcc, s96, v9
	s_and_b64 s[18:19], s[18:19], s[44:45]
	s_and_saveexec_b64 s[44:45], s[18:19]
	v_lshl_add_u32 v14, v3, 3, s88
	ds_write_b64 v14, v[6:7]
	s_or_b64 exec, exec, s[44:45]
	s_and_b64 s[8:9], s[8:9], s[100:101]
	v_cmp_gt_u32_e64 s[100:101], s96, v8
	s_and_saveexec_b64 s[44:45], s[8:9]
	v_lshl_add_u32 v14, v0, 3, s88
	v_add_u32_e32 v4, 0x281, v2
	ds_write_b64 v14, v[4:5]
	s_or_b64 exec, exec, s[44:45]
	s_bcnt1_i32_b64 s8, s[46:47]
	s_bcnt1_i32_b64 s9, s[58:59]
	s_and_b64 s[46:47], s[46:47], vcc
	s_and_saveexec_b64 s[44:45], s[46:47]
	v_lshl_add_u32 v14, v9, 3, s88
	ds_write_b64 v14, v[12:13]
	s_or_b64 exec, exec, s[44:45]
	s_and_b64 s[58:59], s[58:59], s[100:101]
	s_and_saveexec_b64 s[44:45], s[58:59]
	v_lshl_add_u32 v14, v8, 3, s88
	v_add_u32_e32 v10, 0x301, v2
	ds_write_b64 v14, v[10:11]
	s_or_b64 exec, exec, s[44:45]
	s_add_i32 s8, s8, s9
	s_add_i32 s49, s98, s8
	s_branch .Lsel0_post_4

.Lsel0_post_4:
	s_add_i32 s8, s33, 0x380
	s_cmp_gt_i32 s8, s10
	s_cbranch_scc1 .LBB0_1119
.LBB0_1162:
	s_add_i32 s8, s33, 0x400
	s_cmp_gt_i32 s8, s10
	s_cbranch_scc1 .Lsel0_single_6
	s_movk_i32 s96, 0x2c0
	v_and_b32_e32 v7, 0xffff, v57
	v_and_b32_e32 v13, 0xffff, v54
	v_add_u32_e32 v6, 0x380, v2
	v_add_u32_e32 v12, 0x400, v2
	v_lshrrev_b32_e32 v5, 16, v57
	v_lshrrev_b32_e32 v11, 16, v54
	v_cmp_gt_u32_e64 s[44:45], s11, v6
	v_cmp_le_u32_e32 vcc, s93, v7
	v_cmp_le_u32_e64 s[46:47], s93, v5
	v_cmp_gt_u32_e64 s[98:99], s11, v12
	s_and_b64 s[18:19], s[44:45], vcc
	s_and_b64 s[8:9], s[44:45], s[46:47]
	v_cmp_le_u32_e32 vcc, s93, v13
	v_cmp_le_u32_e64 s[44:45], s93, v11
	v_mbcnt_lo_u32_b32 v3, s18, 0
	v_mbcnt_hi_u32_b32 v3, s19, v3
	s_and_b64 s[46:47], s[98:99], vcc
	s_and_b64 s[58:59], s[98:99], s[44:45]
	v_mbcnt_lo_u32_b32 v3, s8, v3
	v_mbcnt_hi_u32_b32 v3, s9, v3
	s_bcnt1_i32_b64 s98, s[18:19]
	s_bcnt1_i32_b64 s99, s[8:9]
	v_mbcnt_lo_u32_b32 v9, s46, 0
	v_mbcnt_hi_u32_b32 v9, s47, v9
	s_add_i32 s98, s98, s99
	v_mbcnt_lo_u32_b32 v9, s58, v9
	v_mbcnt_hi_u32_b32 v9, s59, v9
	v_add_u32_e32 v3, s49, v3
	s_add_i32 s98, s49, s98
	v_cndmask_b32_e64 v0, 0, 1, s[18:19]
	v_add_u32_e32 v9, s98, v9
	v_cndmask_b32_e64 v8, 0, 1, s[46:47]
	v_add_u32_e32 v0, v3, v0
	v_add_u32_e32 v8, v9, v8
	v_cmp_gt_u32_e64 s[44:45], s96, v3
	v_cmp_gt_u32_e64 s[100:101], s96, v0
	v_cmp_gt_u32_e32 vcc, s96, v9
	s_and_b64 s[18:19], s[18:19], s[44:45]
	s_and_saveexec_b64 s[44:45], s[18:19]
	v_lshl_add_u32 v14, v3, 3, s88
	ds_write_b64 v14, v[6:7]
	s_or_b64 exec, exec, s[44:45]
	s_and_b64 s[8:9], s[8:9], s[100:101]
	v_cmp_gt_u32_e64 s[100:101], s96, v8
	s_and_saveexec_b64 s[44:45], s[8:9]
	v_lshl_add_u32 v14, v0, 3, s88
	v_add_u32_e32 v4, 0x381, v2
	ds_write_b64 v14, v[4:5]
	s_or_b64 exec, exec, s[44:45]
	s_bcnt1_i32_b64 s8, s[46:47]
	s_bcnt1_i32_b64 s9, s[58:59]
	s_and_b64 s[46:47], s[46:47], vcc
	s_and_saveexec_b64 s[44:45], s[46:47]
	v_lshl_add_u32 v14, v9, 3, s88
	ds_write_b64 v14, v[12:13]
	s_or_b64 exec, exec, s[44:45]
	s_and_b64 s[58:59], s[58:59], s[100:101]
	s_and_saveexec_b64 s[44:45], s[58:59]
	v_lshl_add_u32 v14, v8, 3, s88
	v_add_u32_e32 v10, 0x401, v2
	ds_write_b64 v14, v[10:11]
	s_or_b64 exec, exec, s[44:45]
	s_add_i32 s8, s8, s9
	s_add_i32 s49, s98, s8
	s_branch .Lsel0_post_6

.Lsel0_post_6:
	s_add_i32 s8, s33, 0x480
	s_cmp_gt_i32 s8, s10
	s_cbranch_scc1 .LBB0_1121
.LBB0_1172:
	s_add_i32 s8, s33, 0x500
	s_cmp_gt_i32 s8, s10
	s_cbranch_scc1 .Lsel0_single_8
	s_movk_i32 s96, 0x2c0
	v_and_b32_e32 v7, 0xffff, v55
	v_and_b32_e32 v13, 0xffff, v52
	v_add_u32_e32 v6, 0x480, v2
	v_add_u32_e32 v12, 0x500, v2
	v_lshrrev_b32_e32 v5, 16, v55
	v_lshrrev_b32_e32 v11, 16, v52
	v_cmp_gt_u32_e64 s[44:45], s11, v6
	v_cmp_le_u32_e32 vcc, s93, v7
	v_cmp_le_u32_e64 s[46:47], s93, v5
	v_cmp_gt_u32_e64 s[98:99], s11, v12
	s_and_b64 s[18:19], s[44:45], vcc
	s_and_b64 s[8:9], s[44:45], s[46:47]
	v_cmp_le_u32_e32 vcc, s93, v13
	v_cmp_le_u32_e64 s[44:45], s93, v11
	v_mbcnt_lo_u32_b32 v3, s18, 0
	v_mbcnt_hi_u32_b32 v3, s19, v3
	s_and_b64 s[46:47], s[98:99], vcc
	s_and_b64 s[58:59], s[98:99], s[44:45]
	v_mbcnt_lo_u32_b32 v3, s8, v3
	v_mbcnt_hi_u32_b32 v3, s9, v3
	s_bcnt1_i32_b64 s98, s[18:19]
	s_bcnt1_i32_b64 s99, s[8:9]
	v_mbcnt_lo_u32_b32 v9, s46, 0
	v_mbcnt_hi_u32_b32 v9, s47, v9
	s_add_i32 s98, s98, s99
	v_mbcnt_lo_u32_b32 v9, s58, v9
	v_mbcnt_hi_u32_b32 v9, s59, v9
	v_add_u32_e32 v3, s49, v3
	s_add_i32 s98, s49, s98
	v_cndmask_b32_e64 v0, 0, 1, s[18:19]
	v_add_u32_e32 v9, s98, v9
	v_cndmask_b32_e64 v8, 0, 1, s[46:47]
	v_add_u32_e32 v0, v3, v0
	v_add_u32_e32 v8, v9, v8
	v_cmp_gt_u32_e64 s[44:45], s96, v3
	v_cmp_gt_u32_e64 s[100:101], s96, v0
	v_cmp_gt_u32_e32 vcc, s96, v9
	s_and_b64 s[18:19], s[18:19], s[44:45]
	s_and_saveexec_b64 s[44:45], s[18:19]
	v_lshl_add_u32 v14, v3, 3, s88
	ds_write_b64 v14, v[6:7]
	s_or_b64 exec, exec, s[44:45]
	s_and_b64 s[8:9], s[8:9], s[100:101]
	v_cmp_gt_u32_e64 s[100:101], s96, v8
	s_and_saveexec_b64 s[44:45], s[8:9]
	v_lshl_add_u32 v14, v0, 3, s88
	v_add_u32_e32 v4, 0x481, v2
	ds_write_b64 v14, v[4:5]
	s_or_b64 exec, exec, s[44:45]
	s_bcnt1_i32_b64 s8, s[46:47]
	s_bcnt1_i32_b64 s9, s[58:59]
	s_and_b64 s[46:47], s[46:47], vcc
	s_and_saveexec_b64 s[44:45], s[46:47]
	v_lshl_add_u32 v14, v9, 3, s88
	ds_write_b64 v14, v[12:13]
	s_or_b64 exec, exec, s[44:45]
	s_and_b64 s[58:59], s[58:59], s[100:101]
	s_and_saveexec_b64 s[44:45], s[58:59]
	v_lshl_add_u32 v14, v8, 3, s88
	v_add_u32_e32 v10, 0x501, v2
	ds_write_b64 v14, v[10:11]
	s_or_b64 exec, exec, s[44:45]
	s_add_i32 s8, s8, s9
	s_add_i32 s49, s98, s8
	s_branch .Lsel0_post_8

.Lsel0_post_8:
	s_add_i32 s8, s33, 0x580
	s_cmp_gt_i32 s8, s10
	s_cbranch_scc1 .LBB0_1123
.LBB0_1182:
	s_add_i32 s8, s33, 0x600
	s_cmp_gt_i32 s8, s10
	s_cbranch_scc1 .Lsel0_single_10
	s_movk_i32 s96, 0x2c0
	v_and_b32_e32 v7, 0xffff, v53
	v_and_b32_e32 v13, 0xffff, v34
	v_add_u32_e32 v6, 0x580, v2
	v_add_u32_e32 v12, 0x600, v2
	v_lshrrev_b32_e32 v5, 16, v53
	v_lshrrev_b32_e32 v11, 16, v34
	v_cmp_gt_u32_e64 s[44:45], s11, v6
	v_cmp_le_u32_e32 vcc, s93, v7
	v_cmp_le_u32_e64 s[46:47], s93, v5
	v_cmp_gt_u32_e64 s[98:99], s11, v12
	s_and_b64 s[18:19], s[44:45], vcc
	s_and_b64 s[8:9], s[44:45], s[46:47]
	v_cmp_le_u32_e32 vcc, s93, v13
	v_cmp_le_u32_e64 s[44:45], s93, v11
	v_mbcnt_lo_u32_b32 v3, s18, 0
	v_mbcnt_hi_u32_b32 v3, s19, v3
	s_and_b64 s[46:47], s[98:99], vcc
	s_and_b64 s[58:59], s[98:99], s[44:45]
	v_mbcnt_lo_u32_b32 v3, s8, v3
	v_mbcnt_hi_u32_b32 v3, s9, v3
	s_bcnt1_i32_b64 s98, s[18:19]
	s_bcnt1_i32_b64 s99, s[8:9]
	v_mbcnt_lo_u32_b32 v9, s46, 0
	v_mbcnt_hi_u32_b32 v9, s47, v9
	s_add_i32 s98, s98, s99
	v_mbcnt_lo_u32_b32 v9, s58, v9
	v_mbcnt_hi_u32_b32 v9, s59, v9
	v_add_u32_e32 v3, s49, v3
	s_add_i32 s98, s49, s98
	v_cndmask_b32_e64 v0, 0, 1, s[18:19]
	v_add_u32_e32 v9, s98, v9
	v_cndmask_b32_e64 v8, 0, 1, s[46:47]
	v_add_u32_e32 v0, v3, v0
	v_add_u32_e32 v8, v9, v8
	v_cmp_gt_u32_e64 s[44:45], s96, v3
	v_cmp_gt_u32_e64 s[100:101], s96, v0
	v_cmp_gt_u32_e32 vcc, s96, v9
	s_and_b64 s[18:19], s[18:19], s[44:45]
	s_and_saveexec_b64 s[44:45], s[18:19]
	v_lshl_add_u32 v14, v3, 3, s88
	ds_write_b64 v14, v[6:7]
	s_or_b64 exec, exec, s[44:45]
	s_and_b64 s[8:9], s[8:9], s[100:101]
	v_cmp_gt_u32_e64 s[100:101], s96, v8
	s_and_saveexec_b64 s[44:45], s[8:9]
	v_lshl_add_u32 v14, v0, 3, s88
	v_add_u32_e32 v4, 0x581, v2
	ds_write_b64 v14, v[4:5]
	s_or_b64 exec, exec, s[44:45]
	s_bcnt1_i32_b64 s8, s[46:47]
	s_bcnt1_i32_b64 s9, s[58:59]
	s_and_b64 s[46:47], s[46:47], vcc
	s_and_saveexec_b64 s[44:45], s[46:47]
	v_lshl_add_u32 v14, v9, 3, s88
	ds_write_b64 v14, v[12:13]
	s_or_b64 exec, exec, s[44:45]
	s_and_b64 s[58:59], s[58:59], s[100:101]
	s_and_saveexec_b64 s[44:45], s[58:59]
	v_lshl_add_u32 v14, v8, 3, s88
	v_add_u32_e32 v10, 0x601, v2
	ds_write_b64 v14, v[10:11]
	s_or_b64 exec, exec, s[44:45]
	s_add_i32 s8, s8, s9
	s_add_i32 s49, s98, s8
	s_branch .Lsel0_post_10

.Lsel0_post_10:
	s_add_i32 s8, s33, 0x680
	s_cmp_gt_i32 s8, s10
	s_cbranch_scc1 .LBB0_1125
.LBB0_1192:
	s_add_i32 s8, s33, 0x700
	s_cmp_gt_i32 s8, s10
	s_cbranch_scc1 .Lsel0_single_12
	s_movk_i32 s96, 0x2c0
	v_and_b32_e32 v7, 0xffff, v35
	v_and_b32_e32 v13, 0xffff, v32
	v_add_u32_e32 v6, 0x680, v2
	v_add_u32_e32 v12, 0x700, v2
	v_lshrrev_b32_e32 v5, 16, v35
	v_lshrrev_b32_e32 v11, 16, v32
	v_cmp_gt_u32_e64 s[44:45], s11, v6
	v_cmp_le_u32_e32 vcc, s93, v7
	v_cmp_le_u32_e64 s[46:47], s93, v5
	v_cmp_gt_u32_e64 s[98:99], s11, v12
	s_and_b64 s[18:19], s[44:45], vcc
	s_and_b64 s[8:9], s[44:45], s[46:47]
	v_cmp_le_u32_e32 vcc, s93, v13
	v_cmp_le_u32_e64 s[44:45], s93, v11
	v_mbcnt_lo_u32_b32 v3, s18, 0
	v_mbcnt_hi_u32_b32 v3, s19, v3
	s_and_b64 s[46:47], s[98:99], vcc
	s_and_b64 s[58:59], s[98:99], s[44:45]
	v_mbcnt_lo_u32_b32 v3, s8, v3
	v_mbcnt_hi_u32_b32 v3, s9, v3
	s_bcnt1_i32_b64 s98, s[18:19]
	s_bcnt1_i32_b64 s99, s[8:9]
	v_mbcnt_lo_u32_b32 v9, s46, 0
	v_mbcnt_hi_u32_b32 v9, s47, v9
	s_add_i32 s98, s98, s99
	v_mbcnt_lo_u32_b32 v9, s58, v9
	v_mbcnt_hi_u32_b32 v9, s59, v9
	v_add_u32_e32 v3, s49, v3
	s_add_i32 s98, s49, s98
	v_cndmask_b32_e64 v0, 0, 1, s[18:19]
	v_add_u32_e32 v9, s98, v9
	v_cndmask_b32_e64 v8, 0, 1, s[46:47]
	v_add_u32_e32 v0, v3, v0
	v_add_u32_e32 v8, v9, v8
	v_cmp_gt_u32_e64 s[44:45], s96, v3
	v_cmp_gt_u32_e64 s[100:101], s96, v0
	v_cmp_gt_u32_e32 vcc, s96, v9
	s_and_b64 s[18:19], s[18:19], s[44:45]
	s_and_saveexec_b64 s[44:45], s[18:19]
	v_lshl_add_u32 v14, v3, 3, s88
	ds_write_b64 v14, v[6:7]
	s_or_b64 exec, exec, s[44:45]
	s_and_b64 s[8:9], s[8:9], s[100:101]
	v_cmp_gt_u32_e64 s[100:101], s96, v8
	s_and_saveexec_b64 s[44:45], s[8:9]
	v_lshl_add_u32 v14, v0, 3, s88
	v_add_u32_e32 v4, 0x681, v2
	ds_write_b64 v14, v[4:5]
	s_or_b64 exec, exec, s[44:45]
	s_bcnt1_i32_b64 s8, s[46:47]
	s_bcnt1_i32_b64 s9, s[58:59]
	s_and_b64 s[46:47], s[46:47], vcc
	s_and_saveexec_b64 s[44:45], s[46:47]
	v_lshl_add_u32 v14, v9, 3, s88
	ds_write_b64 v14, v[12:13]
	s_or_b64 exec, exec, s[44:45]
	s_and_b64 s[58:59], s[58:59], s[100:101]
	s_and_saveexec_b64 s[44:45], s[58:59]
	v_lshl_add_u32 v14, v8, 3, s88
	v_add_u32_e32 v10, 0x701, v2
	ds_write_b64 v14, v[10:11]
	s_or_b64 exec, exec, s[44:45]
	s_add_i32 s8, s8, s9
	s_add_i32 s49, s98, s8
	s_branch .Lsel0_post_12

.Lsel0_post_12:
	s_add_i32 s8, s33, 0x780
	s_cmp_gt_i32 s8, s10
	s_cbranch_scc1 .LBB0_1207

.LBB0_1235:
	s_add_i32 s8, s30, 0x100
	s_cmp_gt_i32 s8, s10
	s_cbranch_scc1 .Lsel1_single_0
	s_movk_i32 s96, 0x2c0
	v_and_b32_e32 v7, 0xffff, v17
	v_and_b32_e32 v13, 0xffff, v18
	v_add_u32_e32 v6, 0x80, v2
	v_add_u32_e32 v12, 0x100, v2
	v_lshrrev_b32_e32 v5, 16, v17
	v_lshrrev_b32_e32 v11, 16, v18
	v_cmp_gt_u32_e64 s[44:45], s11, v6
	v_cmp_le_u32_e32 vcc, s29, v7
	v_cmp_le_u32_e64 s[46:47], s29, v5
	v_cmp_gt_u32_e64 s[98:99], s11, v12
	s_and_b64 s[18:19], s[44:45], vcc
	s_and_b64 s[8:9], s[44:45], s[46:47]
	v_cmp_le_u32_e32 vcc, s29, v13
	v_cmp_le_u32_e64 s[44:45], s29, v11
	v_mbcnt_lo_u32_b32 v3, s18, 0
	v_mbcnt_hi_u32_b32 v3, s19, v3
	s_and_b64 s[46:47], s[98:99], vcc
	s_and_b64 s[58:59], s[98:99], s[44:45]
	v_mbcnt_lo_u32_b32 v3, s8, v3
	v_mbcnt_hi_u32_b32 v3, s9, v3
	s_bcnt1_i32_b64 s98, s[18:19]
	s_bcnt1_i32_b64 s99, s[8:9]
	v_mbcnt_lo_u32_b32 v9, s46, 0
	v_mbcnt_hi_u32_b32 v9, s47, v9
	s_add_i32 s98, s98, s99
	v_mbcnt_lo_u32_b32 v9, s58, v9
	v_mbcnt_hi_u32_b32 v9, s59, v9
	v_add_u32_e32 v3, s28, v3
	s_add_i32 s98, s28, s98
	v_cndmask_b32_e64 v0, 0, 1, s[18:19]
	v_add_u32_e32 v9, s98, v9
	v_cndmask_b32_e64 v8, 0, 1, s[46:47]
	v_add_u32_e32 v0, v3, v0
	v_add_u32_e32 v8, v9, v8
	v_cmp_gt_u32_e64 s[44:45], s96, v3
	v_cmp_gt_u32_e64 s[100:101], s96, v0
	v_cmp_gt_u32_e32 vcc, s96, v9
	s_and_b64 s[18:19], s[18:19], s[44:45]
	s_and_saveexec_b64 s[44:45], s[18:19]
	v_lshl_add_u32 v14, v3, 3, s88
	ds_write_b64 v14, v[6:7]
	s_or_b64 exec, exec, s[44:45]
	s_and_b64 s[8:9], s[8:9], s[100:101]
	v_cmp_gt_u32_e64 s[100:101], s96, v8
	s_and_saveexec_b64 s[44:45], s[8:9]
	v_lshl_add_u32 v14, v0, 3, s88
	v_add_u32_e32 v4, 0x81, v2
	ds_write_b64 v14, v[4:5]
	s_or_b64 exec, exec, s[44:45]
	s_bcnt1_i32_b64 s8, s[46:47]
	s_bcnt1_i32_b64 s9, s[58:59]
	s_and_b64 s[46:47], s[46:47], vcc
	s_and_saveexec_b64 s[44:45], s[46:47]
	v_lshl_add_u32 v14, v9, 3, s88
	ds_write_b64 v14, v[12:13]
	s_or_b64 exec, exec, s[44:45]
	s_and_b64 s[58:59], s[58:59], s[100:101]
	s_and_saveexec_b64 s[44:45], s[58:59]
	v_lshl_add_u32 v14, v8, 3, s88
	v_add_u32_e32 v10, 0x101, v2
	ds_write_b64 v14, v[10:11]
	s_or_b64 exec, exec, s[44:45]
	s_add_i32 s8, s8, s9
	s_add_i32 s28, s98, s8
	s_branch .Lsel1_post_0

.Lsel1_post_0:
	s_add_i32 s8, s30, 0x180
	s_cmp_gt_i32 s8, s10
	s_cbranch_scc1 .LBB0_1218
.LBB0_1245:
	s_add_i32 s8, s30, 0x200
	s_cmp_gt_i32 s8, s10
	s_cbranch_scc1 .Lsel1_single_2
	s_movk_i32 s96, 0x2c0
	v_and_b32_e32 v7, 0xffff, v19
	v_and_b32_e32 v13, 0xffff, v20
	v_add_u32_e32 v6, 0x180, v2
	v_add_u32_e32 v12, 0x200, v2
	v_lshrrev_b32_e32 v5, 16, v19
	v_lshrrev_b32_e32 v11, 16, v20
	v_cmp_gt_u32_e64 s[44:45], s11, v6
	v_cmp_le_u32_e32 vcc, s29, v7
	v_cmp_le_u32_e64 s[46:47], s29, v5
	v_cmp_gt_u32_e64 s[98:99], s11, v12
	s_and_b64 s[18:19], s[44:45], vcc
	s_and_b64 s[8:9], s[44:45], s[46:47]
	v_cmp_le_u32_e32 vcc, s29, v13
	v_cmp_le_u32_e64 s[44:45], s29, v11
	v_mbcnt_lo_u32_b32 v3, s18, 0
	v_mbcnt_hi_u32_b32 v3, s19, v3
	s_and_b64 s[46:47], s[98:99], vcc
	s_and_b64 s[58:59], s[98:99], s[44:45]
	v_mbcnt_lo_u32_b32 v3, s8, v3
	v_mbcnt_hi_u32_b32 v3, s9, v3
	s_bcnt1_i32_b64 s98, s[18:19]
	s_bcnt1_i32_b64 s99, s[8:9]
	v_mbcnt_lo_u32_b32 v9, s46, 0
	v_mbcnt_hi_u32_b32 v9, s47, v9
	s_add_i32 s98, s98, s99
	v_mbcnt_lo_u32_b32 v9, s58, v9
	v_mbcnt_hi_u32_b32 v9, s59, v9
	v_add_u32_e32 v3, s28, v3
	s_add_i32 s98, s28, s98
	v_cndmask_b32_e64 v0, 0, 1, s[18:19]
	v_add_u32_e32 v9, s98, v9
	v_cndmask_b32_e64 v8, 0, 1, s[46:47]
	v_add_u32_e32 v0, v3, v0
	v_add_u32_e32 v8, v9, v8
	v_cmp_gt_u32_e64 s[44:45], s96, v3
	v_cmp_gt_u32_e64 s[100:101], s96, v0
	v_cmp_gt_u32_e32 vcc, s96, v9
	s_and_b64 s[18:19], s[18:19], s[44:45]
	s_and_saveexec_b64 s[44:45], s[18:19]
	v_lshl_add_u32 v14, v3, 3, s88
	ds_write_b64 v14, v[6:7]
	s_or_b64 exec, exec, s[44:45]
	s_and_b64 s[8:9], s[8:9], s[100:101]
	v_cmp_gt_u32_e64 s[100:101], s96, v8
	s_and_saveexec_b64 s[44:45], s[8:9]
	v_lshl_add_u32 v14, v0, 3, s88
	v_add_u32_e32 v4, 0x181, v2
	ds_write_b64 v14, v[4:5]
	s_or_b64 exec, exec, s[44:45]
	s_bcnt1_i32_b64 s8, s[46:47]
	s_bcnt1_i32_b64 s9, s[58:59]
	s_and_b64 s[46:47], s[46:47], vcc
	s_and_saveexec_b64 s[44:45], s[46:47]
	v_lshl_add_u32 v14, v9, 3, s88
	ds_write_b64 v14, v[12:13]
	s_or_b64 exec, exec, s[44:45]
	s_and_b64 s[58:59], s[58:59], s[100:101]
	s_and_saveexec_b64 s[44:45], s[58:59]
	v_lshl_add_u32 v14, v8, 3, s88
	v_add_u32_e32 v10, 0x201, v2
	ds_write_b64 v14, v[10:11]
	s_or_b64 exec, exec, s[44:45]
	s_add_i32 s8, s8, s9
	s_add_i32 s28, s98, s8
	s_branch .Lsel1_post_2

.Lsel1_post_2:
	s_add_i32 s8, s30, 0x280
	s_cmp_gt_i32 s8, s10
	s_cbranch_scc1 .LBB0_1220
.LBB0_1255:
	s_add_i32 s8, s30, 0x300
	s_cmp_gt_i32 s8, s10
	s_cbranch_scc1 .Lsel1_single_4
	s_movk_i32 s96, 0x2c0
	v_and_b32_e32 v7, 0xffff, v21
	v_and_b32_e32 v13, 0xffff, v22
	v_add_u32_e32 v6, 0x280, v2
	v_add_u32_e32 v12, 0x300, v2
	v_lshrrev_b32_e32 v5, 16, v21
	v_lshrrev_b32_e32 v11, 16, v22
	v_cmp_gt_u32_e64 s[44:45], s11, v6
	v_cmp_le_u32_e32 vcc, s29, v7
	v_cmp_le_u32_e64 s[46:47], s29, v5
	v_cmp_gt_u32_e64 s[98:99], s11, v12
	s_and_b64 s[18:19], s[44:45], vcc
	s_and_b64 s[8:9], s[44:45], s[46:47]
	v_cmp_le_u32_e32 vcc, s29, v13
	v_cmp_le_u32_e64 s[44:45], s29, v11
	v_mbcnt_lo_u32_b32 v3, s18, 0
	v_mbcnt_hi_u32_b32 v3, s19, v3
	s_and_b64 s[46:47], s[98:99], vcc
	s_and_b64 s[58:59], s[98:99], s[44:45]
	v_mbcnt_lo_u32_b32 v3, s8, v3
	v_mbcnt_hi_u32_b32 v3, s9, v3
	s_bcnt1_i32_b64 s98, s[18:19]
	s_bcnt1_i32_b64 s99, s[8:9]
	v_mbcnt_lo_u32_b32 v9, s46, 0
	v_mbcnt_hi_u32_b32 v9, s47, v9
	s_add_i32 s98, s98, s99
	v_mbcnt_lo_u32_b32 v9, s58, v9
	v_mbcnt_hi_u32_b32 v9, s59, v9
	v_add_u32_e32 v3, s28, v3
	s_add_i32 s98, s28, s98
	v_cndmask_b32_e64 v0, 0, 1, s[18:19]
	v_add_u32_e32 v9, s98, v9
	v_cndmask_b32_e64 v8, 0, 1, s[46:47]
	v_add_u32_e32 v0, v3, v0
	v_add_u32_e32 v8, v9, v8
	v_cmp_gt_u32_e64 s[44:45], s96, v3
	v_cmp_gt_u32_e64 s[100:101], s96, v0
	v_cmp_gt_u32_e32 vcc, s96, v9
	s_and_b64 s[18:19], s[18:19], s[44:45]
	s_and_saveexec_b64 s[44:45], s[18:19]
	v_lshl_add_u32 v14, v3, 3, s88
	ds_write_b64 v14, v[6:7]
	s_or_b64 exec, exec, s[44:45]
	s_and_b64 s[8:9], s[8:9], s[100:101]
	v_cmp_gt_u32_e64 s[100:101], s96, v8
	s_and_saveexec_b64 s[44:45], s[8:9]
	v_lshl_add_u32 v14, v0, 3, s88
	v_add_u32_e32 v4, 0x281, v2
	ds_write_b64 v14, v[4:5]
	s_or_b64 exec, exec, s[44:45]
	s_bcnt1_i32_b64 s8, s[46:47]
	s_bcnt1_i32_b64 s9, s[58:59]
	s_and_b64 s[46:47], s[46:47], vcc
	s_and_saveexec_b64 s[44:45], s[46:47]
	v_lshl_add_u32 v14, v9, 3, s88
	ds_write_b64 v14, v[12:13]
	s_or_b64 exec, exec, s[44:45]
	s_and_b64 s[58:59], s[58:59], s[100:101]
	s_and_saveexec_b64 s[44:45], s[58:59]
	v_lshl_add_u32 v14, v8, 3, s88
	v_add_u32_e32 v10, 0x301, v2
	ds_write_b64 v14, v[10:11]
	s_or_b64 exec, exec, s[44:45]
	s_add_i32 s8, s8, s9
	s_add_i32 s28, s98, s8
	s_branch .Lsel1_post_4

.Lsel1_post_4:
	s_add_i32 s8, s30, 0x380
	s_cmp_gt_i32 s8, s10
	s_cbranch_scc1 .LBB0_1222
.LBB0_1265:
	s_add_i32 s8, s30, 0x400
	s_cmp_gt_i32 s8, s10
	s_cbranch_scc1 .Lsel1_single_6
	s_movk_i32 s96, 0x2c0
	v_and_b32_e32 v7, 0xffff, v23
	v_and_b32_e32 v13, 0xffff, v24
	v_add_u32_e32 v6, 0x380, v2
	v_add_u32_e32 v12, 0x400, v2
	v_lshrrev_b32_e32 v5, 16, v23
	v_lshrrev_b32_e32 v11, 16, v24
	v_cmp_gt_u32_e64 s[44:45], s11, v6
	v_cmp_le_u32_e32 vcc, s29, v7
	v_cmp_le_u32_e64 s[46:47], s29, v5
	v_cmp_gt_u32_e64 s[98:99], s11, v12
	s_and_b64 s[18:19], s[44:45], vcc
	s_and_b64 s[8:9], s[44:45], s[46:47]
	v_cmp_le_u32_e32 vcc, s29, v13
	v_cmp_le_u32_e64 s[44:45], s29, v11
	v_mbcnt_lo_u32_b32 v3, s18, 0
	v_mbcnt_hi_u32_b32 v3, s19, v3
	s_and_b64 s[46:47], s[98:99], vcc
	s_and_b64 s[58:59], s[98:99], s[44:45]
	v_mbcnt_lo_u32_b32 v3, s8, v3
	v_mbcnt_hi_u32_b32 v3, s9, v3
	s_bcnt1_i32_b64 s98, s[18:19]
	s_bcnt1_i32_b64 s99, s[8:9]
	v_mbcnt_lo_u32_b32 v9, s46, 0
	v_mbcnt_hi_u32_b32 v9, s47, v9
	s_add_i32 s98, s98, s99
	v_mbcnt_lo_u32_b32 v9, s58, v9
	v_mbcnt_hi_u32_b32 v9, s59, v9
	v_add_u32_e32 v3, s28, v3
	s_add_i32 s98, s28, s98
	v_cndmask_b32_e64 v0, 0, 1, s[18:19]
	v_add_u32_e32 v9, s98, v9
	v_cndmask_b32_e64 v8, 0, 1, s[46:47]
	v_add_u32_e32 v0, v3, v0
	v_add_u32_e32 v8, v9, v8
	v_cmp_gt_u32_e64 s[44:45], s96, v3
	v_cmp_gt_u32_e64 s[100:101], s96, v0
	v_cmp_gt_u32_e32 vcc, s96, v9
	s_and_b64 s[18:19], s[18:19], s[44:45]
	s_and_saveexec_b64 s[44:45], s[18:19]
	v_lshl_add_u32 v14, v3, 3, s88
	ds_write_b64 v14, v[6:7]
	s_or_b64 exec, exec, s[44:45]
	s_and_b64 s[8:9], s[8:9], s[100:101]
	v_cmp_gt_u32_e64 s[100:101], s96, v8
	s_and_saveexec_b64 s[44:45], s[8:9]
	v_lshl_add_u32 v14, v0, 3, s88
	v_add_u32_e32 v4, 0x381, v2
	ds_write_b64 v14, v[4:5]
	s_or_b64 exec, exec, s[44:45]
	s_bcnt1_i32_b64 s8, s[46:47]
	s_bcnt1_i32_b64 s9, s[58:59]
	s_and_b64 s[46:47], s[46:47], vcc
	s_and_saveexec_b64 s[44:45], s[46:47]
	v_lshl_add_u32 v14, v9, 3, s88
	ds_write_b64 v14, v[12:13]
	s_or_b64 exec, exec, s[44:45]
	s_and_b64 s[58:59], s[58:59], s[100:101]
	s_and_saveexec_b64 s[44:45], s[58:59]
	v_lshl_add_u32 v14, v8, 3, s88
	v_add_u32_e32 v10, 0x401, v2
	ds_write_b64 v14, v[10:11]
	s_or_b64 exec, exec, s[44:45]
	s_add_i32 s8, s8, s9
	s_add_i32 s28, s98, s8
	s_branch .Lsel1_post_6

.Lsel1_post_6:
	s_add_i32 s8, s30, 0x480
	s_cmp_gt_i32 s8, s10
	s_cbranch_scc1 .LBB0_1224
.LBB0_1275:
	s_add_i32 s8, s30, 0x500
	s_cmp_gt_i32 s8, s10
	s_cbranch_scc1 .Lsel1_single_8
	s_movk_i32 s96, 0x2c0
	v_and_b32_e32 v7, 0xffff, v25
	v_and_b32_e32 v13, 0xffff, v26
	v_add_u32_e32 v6, 0x480, v2
	v_add_u32_e32 v12, 0x500, v2
	v_lshrrev_b32_e32 v5, 16, v25
	v_lshrrev_b32_e32 v11, 16, v26
	v_cmp_gt_u32_e64 s[44:45], s11, v6
	v_cmp_le_u32_e32 vcc, s29, v7
	v_cmp_le_u32_e64 s[46:47], s29, v5
	v_cmp_gt_u32_e64 s[98:99], s11, v12
	s_and_b64 s[18:19], s[44:45], vcc
	s_and_b64 s[8:9], s[44:45], s[46:47]
	v_cmp_le_u32_e32 vcc, s29, v13
	v_cmp_le_u32_e64 s[44:45], s29, v11
	v_mbcnt_lo_u32_b32 v3, s18, 0
	v_mbcnt_hi_u32_b32 v3, s19, v3
	s_and_b64 s[46:47], s[98:99], vcc
	s_and_b64 s[58:59], s[98:99], s[44:45]
	v_mbcnt_lo_u32_b32 v3, s8, v3
	v_mbcnt_hi_u32_b32 v3, s9, v3
	s_bcnt1_i32_b64 s98, s[18:19]
	s_bcnt1_i32_b64 s99, s[8:9]
	v_mbcnt_lo_u32_b32 v9, s46, 0
	v_mbcnt_hi_u32_b32 v9, s47, v9
	s_add_i32 s98, s98, s99
	v_mbcnt_lo_u32_b32 v9, s58, v9
	v_mbcnt_hi_u32_b32 v9, s59, v9
	v_add_u32_e32 v3, s28, v3
	s_add_i32 s98, s28, s98
	v_cndmask_b32_e64 v0, 0, 1, s[18:19]
	v_add_u32_e32 v9, s98, v9
	v_cndmask_b32_e64 v8, 0, 1, s[46:47]
	v_add_u32_e32 v0, v3, v0
	v_add_u32_e32 v8, v9, v8
	v_cmp_gt_u32_e64 s[44:45], s96, v3
	v_cmp_gt_u32_e64 s[100:101], s96, v0
	v_cmp_gt_u32_e32 vcc, s96, v9
	s_and_b64 s[18:19], s[18:19], s[44:45]
	s_and_saveexec_b64 s[44:45], s[18:19]
	v_lshl_add_u32 v14, v3, 3, s88
	ds_write_b64 v14, v[6:7]
	s_or_b64 exec, exec, s[44:45]
	s_and_b64 s[8:9], s[8:9], s[100:101]
	v_cmp_gt_u32_e64 s[100:101], s96, v8
	s_and_saveexec_b64 s[44:45], s[8:9]
	v_lshl_add_u32 v14, v0, 3, s88
	v_add_u32_e32 v4, 0x481, v2
	ds_write_b64 v14, v[4:5]
	s_or_b64 exec, exec, s[44:45]
	s_bcnt1_i32_b64 s8, s[46:47]
	s_bcnt1_i32_b64 s9, s[58:59]
	s_and_b64 s[46:47], s[46:47], vcc
	s_and_saveexec_b64 s[44:45], s[46:47]
	v_lshl_add_u32 v14, v9, 3, s88
	ds_write_b64 v14, v[12:13]
	s_or_b64 exec, exec, s[44:45]
	s_and_b64 s[58:59], s[58:59], s[100:101]
	s_and_saveexec_b64 s[44:45], s[58:59]
	v_lshl_add_u32 v14, v8, 3, s88
	v_add_u32_e32 v10, 0x501, v2
	ds_write_b64 v14, v[10:11]
	s_or_b64 exec, exec, s[44:45]
	s_add_i32 s8, s8, s9
	s_add_i32 s28, s98, s8
	s_branch .Lsel1_post_8

.Lsel1_post_8:
	s_add_i32 s8, s30, 0x580
	s_cmp_gt_i32 s8, s10
	s_cbranch_scc1 .LBB0_1226
.LBB0_1285:
	s_add_i32 s8, s30, 0x600
	s_cmp_gt_i32 s8, s10
	s_cbranch_scc1 .Lsel1_single_10
	s_movk_i32 s96, 0x2c0
	v_and_b32_e32 v7, 0xffff, v27
	v_and_b32_e32 v13, 0xffff, v28
	v_add_u32_e32 v6, 0x580, v2
	v_add_u32_e32 v12, 0x600, v2
	v_lshrrev_b32_e32 v5, 16, v27
	v_lshrrev_b32_e32 v11, 16, v28
	v_cmp_gt_u32_e64 s[44:45], s11, v6
	v_cmp_le_u32_e32 vcc, s29, v7
	v_cmp_le_u32_e64 s[46:47], s29, v5
	v_cmp_gt_u32_e64 s[98:99], s11, v12
	s_and_b64 s[18:19], s[44:45], vcc
	s_and_b64 s[8:9], s[44:45], s[46:47]
	v_cmp_le_u32_e32 vcc, s29, v13
	v_cmp_le_u32_e64 s[44:45], s29, v11
	v_mbcnt_lo_u32_b32 v3, s18, 0
	v_mbcnt_hi_u32_b32 v3, s19, v3
	s_and_b64 s[46:47], s[98:99], vcc
	s_and_b64 s[58:59], s[98:99], s[44:45]
	v_mbcnt_lo_u32_b32 v3, s8, v3
	v_mbcnt_hi_u32_b32 v3, s9, v3
	s_bcnt1_i32_b64 s98, s[18:19]
	s_bcnt1_i32_b64 s99, s[8:9]
	v_mbcnt_lo_u32_b32 v9, s46, 0
	v_mbcnt_hi_u32_b32 v9, s47, v9
	s_add_i32 s98, s98, s99
	v_mbcnt_lo_u32_b32 v9, s58, v9
	v_mbcnt_hi_u32_b32 v9, s59, v9
	v_add_u32_e32 v3, s28, v3
	s_add_i32 s98, s28, s98
	v_cndmask_b32_e64 v0, 0, 1, s[18:19]
	v_add_u32_e32 v9, s98, v9
	v_cndmask_b32_e64 v8, 0, 1, s[46:47]
	v_add_u32_e32 v0, v3, v0
	v_add_u32_e32 v8, v9, v8
	v_cmp_gt_u32_e64 s[44:45], s96, v3
	v_cmp_gt_u32_e64 s[100:101], s96, v0
	v_cmp_gt_u32_e32 vcc, s96, v9
	s_and_b64 s[18:19], s[18:19], s[44:45]
	s_and_saveexec_b64 s[44:45], s[18:19]
	v_lshl_add_u32 v14, v3, 3, s88
	ds_write_b64 v14, v[6:7]
	s_or_b64 exec, exec, s[44:45]
	s_and_b64 s[8:9], s[8:9], s[100:101]
	v_cmp_gt_u32_e64 s[100:101], s96, v8
	s_and_saveexec_b64 s[44:45], s[8:9]
	v_lshl_add_u32 v14, v0, 3, s88
	v_add_u32_e32 v4, 0x581, v2
	ds_write_b64 v14, v[4:5]
	s_or_b64 exec, exec, s[44:45]
	s_bcnt1_i32_b64 s8, s[46:47]
	s_bcnt1_i32_b64 s9, s[58:59]
	s_and_b64 s[46:47], s[46:47], vcc
	s_and_saveexec_b64 s[44:45], s[46:47]
	v_lshl_add_u32 v14, v9, 3, s88
	ds_write_b64 v14, v[12:13]
	s_or_b64 exec, exec, s[44:45]
	s_and_b64 s[58:59], s[58:59], s[100:101]
	s_and_saveexec_b64 s[44:45], s[58:59]
	v_lshl_add_u32 v14, v8, 3, s88
	v_add_u32_e32 v10, 0x601, v2
	ds_write_b64 v14, v[10:11]
	s_or_b64 exec, exec, s[44:45]
	s_add_i32 s8, s8, s9
	s_add_i32 s28, s98, s8
	s_branch .Lsel1_post_10

.Lsel1_post_10:
	s_add_i32 s8, s30, 0x680
	s_cmp_gt_i32 s8, s10
	s_cbranch_scc1 .LBB0_1228
.LBB0_1295:
	s_add_i32 s8, s30, 0x700
	s_cmp_gt_i32 s8, s10
	s_cbranch_scc1 .Lsel1_single_12
	s_movk_i32 s96, 0x2c0
	v_and_b32_e32 v7, 0xffff, v29
	v_and_b32_e32 v13, 0xffff, v30
	v_add_u32_e32 v6, 0x680, v2
	v_add_u32_e32 v12, 0x700, v2
	v_lshrrev_b32_e32 v5, 16, v29
	v_lshrrev_b32_e32 v11, 16, v30
	v_cmp_gt_u32_e64 s[44:45], s11, v6
	v_cmp_le_u32_e32 vcc, s29, v7
	v_cmp_le_u32_e64 s[46:47], s29, v5
	v_cmp_gt_u32_e64 s[98:99], s11, v12
	s_and_b64 s[18:19], s[44:45], vcc
	s_and_b64 s[8:9], s[44:45], s[46:47]
	v_cmp_le_u32_e32 vcc, s29, v13
	v_cmp_le_u32_e64 s[44:45], s29, v11
	v_mbcnt_lo_u32_b32 v3, s18, 0
	v_mbcnt_hi_u32_b32 v3, s19, v3
	s_and_b64 s[46:47], s[98:99], vcc
	s_and_b64 s[58:59], s[98:99], s[44:45]
	v_mbcnt_lo_u32_b32 v3, s8, v3
	v_mbcnt_hi_u32_b32 v3, s9, v3
	s_bcnt1_i32_b64 s98, s[18:19]
	s_bcnt1_i32_b64 s99, s[8:9]
	v_mbcnt_lo_u32_b32 v9, s46, 0
	v_mbcnt_hi_u32_b32 v9, s47, v9
	s_add_i32 s98, s98, s99
	v_mbcnt_lo_u32_b32 v9, s58, v9
	v_mbcnt_hi_u32_b32 v9, s59, v9
	v_add_u32_e32 v3, s28, v3
	s_add_i32 s98, s28, s98
	v_cndmask_b32_e64 v0, 0, 1, s[18:19]
	v_add_u32_e32 v9, s98, v9
	v_cndmask_b32_e64 v8, 0, 1, s[46:47]
	v_add_u32_e32 v0, v3, v0
	v_add_u32_e32 v8, v9, v8
	v_cmp_gt_u32_e64 s[44:45], s96, v3
	v_cmp_gt_u32_e64 s[100:101], s96, v0
	v_cmp_gt_u32_e32 vcc, s96, v9
	s_and_b64 s[18:19], s[18:19], s[44:45]
	s_and_saveexec_b64 s[44:45], s[18:19]
	v_lshl_add_u32 v14, v3, 3, s88
	ds_write_b64 v14, v[6:7]
	s_or_b64 exec, exec, s[44:45]
	s_and_b64 s[8:9], s[8:9], s[100:101]
	v_cmp_gt_u32_e64 s[100:101], s96, v8
	s_and_saveexec_b64 s[44:45], s[8:9]
	v_lshl_add_u32 v14, v0, 3, s88
	v_add_u32_e32 v4, 0x681, v2
	ds_write_b64 v14, v[4:5]
	s_or_b64 exec, exec, s[44:45]
	s_bcnt1_i32_b64 s8, s[46:47]
	s_bcnt1_i32_b64 s9, s[58:59]
	s_and_b64 s[46:47], s[46:47], vcc
	s_and_saveexec_b64 s[44:45], s[46:47]
	v_lshl_add_u32 v14, v9, 3, s88
	ds_write_b64 v14, v[12:13]
	s_or_b64 exec, exec, s[44:45]
	s_and_b64 s[58:59], s[58:59], s[100:101]
	s_and_saveexec_b64 s[44:45], s[58:59]
	v_lshl_add_u32 v14, v8, 3, s88
	v_add_u32_e32 v10, 0x701, v2
	ds_write_b64 v14, v[10:11]
	s_or_b64 exec, exec, s[44:45]
	s_add_i32 s8, s8, s9
	s_add_i32 s28, s98, s8
	s_branch .Lsel1_post_12

.Lsel1_post_12:
	s_add_i32 s8, s30, 0x780
	s_cmp_gt_i32 s8, s10
	s_cbranch_scc1 .LBB0_1310

	.amdhsa_kernel _Z6mk_fwd4Args
		.amdhsa_group_segment_fixed_size 0
		.amdhsa_private_segment_fixed_size 0
		.amdhsa_kernarg_size 440
		.amdhsa_user_sgpr_count 2
		.amdhsa_user_sgpr_dispatch_ptr 0
		.amdhsa_user_sgpr_queue_ptr 0
		.amdhsa_user_sgpr_kernarg_segment_ptr 1
		.amdhsa_user_sgpr_dispatch_id 0
		.amdhsa_user_sgpr_kernarg_preload_length 0
		.amdhsa_user_sgpr_kernarg_preload_offset 0
		.amdhsa_user_sgpr_private_segment_size 0
		.amdhsa_uses_dynamic_stack 0
		.amdhsa_enable_private_segment 0
		.amdhsa_system_sgpr_workgroup_id_x 1
		.amdhsa_system_sgpr_workgroup_id_y 0
		.amdhsa_system_sgpr_workgroup_id_z 0
		.amdhsa_system_sgpr_workgroup_info 0
		.amdhsa_system_vgpr_workitem_id 0
		.amdhsa_next_free_vgpr 256
		.amdhsa_next_free_sgpr 102
		.amdhsa_accum_offset 256
		.amdhsa_reserve_vcc 1
		.amdhsa_float_round_mode_32 0
		.amdhsa_float_round_mode_16_64 0
		.amdhsa_float_denorm_mode_32 3
		.amdhsa_float_denorm_mode_16_64 3
		.amdhsa_dx10_clamp 1
		.amdhsa_ieee_mode 1
		.amdhsa_fp16_overflow 0
		.amdhsa_tg_split 0
		.amdhsa_exception_fp_ieee_invalid_op 0
		.amdhsa_exception_fp_denorm_src 0
		.amdhsa_exception_fp_ieee_div_zero 0
		.amdhsa_exception_fp_ieee_overflow 0
		.amdhsa_exception_fp_ieee_underflow 0
		.amdhsa_exception_fp_ieee_inexact 0
		.amdhsa_exception_int_div_zero 0
	.end_amdhsa_kernel

amdhsa.kernels:
  - .agpr_count:     0
    .args:
      - .offset:         0
        .size:           184
        .value_kind:     by_value
      - .offset:         184
        .size:           4
        .value_kind:     hidden_block_count_x
      - .offset:         188
        .size:           4
        .value_kind:     hidden_block_count_y
      - .offset:         192
        .size:           4
        .value_kind:     hidden_block_count_z
      - .offset:         196
        .size:           2
        .value_kind:     hidden_group_size_x
      - .offset:         198
        .size:           2
        .value_kind:     hidden_group_size_y
      - .offset:         200
        .size:           2
        .value_kind:     hidden_group_size_z
      - .offset:         202
        .size:           2
        .value_kind:     hidden_remainder_x
      - .offset:         204
        .size:           2
        .value_kind:     hidden_remainder_y
      - .offset:         206
        .size:           2
        .value_kind:     hidden_remainder_z
      - .offset:         224
        .size:           8
        .value_kind:     hidden_global_offset_x
      - .offset:         232
        .size:           8
        .value_kind:     hidden_global_offset_y
      - .offset:         240
        .size:           8
        .value_kind:     hidden_global_offset_z
      - .offset:         248
        .size:           2
        .value_kind:     hidden_grid_dims
      - .offset:         304
        .size:           4
        .value_kind:     hidden_dynamic_lds_size
    .group_segment_fixed_size: 0
    .kernarg_segment_align: 8
    .kernarg_segment_size: 440
    .language:       OpenCL C
    .language_version:
      - 2
      - 0
    .max_flat_workgroup_size: 512
    .name:           _Z6mk_fwd4Args
    .private_segment_fixed_size: 0
    .sgpr_count:     108
    .sgpr_spill_count: 252
    .symbol:         _Z6mk_fwd4Args.kd
    .uniform_work_group_size: 1
    .uses_dynamic_stack: false
    .vgpr_count:     256
    .vgpr_spill_count: 0
    .wavefront_size: 64
